# P0 fp8 weight (W8) stores: sc1 + nt (write-through and streaming; consumed only in P5/P6)
# speedup vs baseline: 1.0054x; 1.0010x over previous
.LBB0_16:
	v_readfirstlane_b32 s50, v18
	s_lshl_b32 s51, s8, 12
	s_lshl_b32 s50, s50, 2
	s_add_u32 s50, s50, s51
	s_add_u32 s56, s6, s50
	s_addc_u32 s57, s7, 0
	v_and_b32_e32 v100, 3, v36
	v_lshrrev_b32_e32 v101, 5, v36
	v_lshl_or_b32 v100, v101, 2, v100
	v_bfe_u32 v101, v36, 2, 3
	v_lshlrev_b32_e32 v102, 12, v100
	v_lshl_or_b32 v102, v101, 4, v102
	v_lshlrev_b32_e32 v103, 2, v6
	v_sub_u32_e32 v103, v8, v103
	v_mad_u32_u24 v103, v100, s15, v103
	v_lshl_add_u32 v103, v101, 4, v103
	global_load_dwordx4 v[120:123], v102, s[56:57] nt
	s_add_u32 s56, s56, 0x8000
	s_addc_u32 s57, s57, 0
	global_load_dwordx4 v[124:127], v102, s[56:57] nt
	s_add_u32 s56, s56, 0x8000
	s_addc_u32 s57, s57, 0
	s_cmp_lg_u32 s60, 0
	s_cbranch_scc0 .Lnp_dn
	global_store_dwordx4 v[164:165], v[160:163], off sc1 nt
	global_store_dwordx4 v[170:171], v[166:169], off sc1 nt
	s_waitcnt vmcnt(2)
	s_branch .Ljoin_dn

.Lks_done:
	global_load_dwordx4 v[120:123], v102, s[56:57] nt
	s_add_u32 s56, s56, 0x10000
	s_addc_u32 s57, s57, 0
	global_load_dwordx4 v[124:127], v102, s[56:57] nt
	s_add_u32 s56, s56, 0x10000
	s_addc_u32 s57, s57, 0
	s_cmp_lg_u32 s60, 0
	s_cbranch_scc0 .Lnp_gu
	global_store_dwordx4 v[164:165], v[160:163], off sc1 nt
	global_store_dwordx4 v[170:171], v[166:169], off sc1 nt
	s_waitcnt vmcnt(2)
	s_branch .Ljoin_gu

.LBB0_31:
	s_cmp_lg_u32 s60, 0
	s_cbranch_scc0 .Lnoflush
	global_store_dwordx4 v[164:165], v[160:163], off sc1 nt
	global_store_dwordx4 v[170:171], v[166:169], off sc1 nt
